# baseline (speedup 1.0000x reference)
.Lep_wait:
	ds_read_b32 v64, v63
	s_waitcnt lgkmcnt(0)
	v_readfirstlane_b32 s95, v64
	s_cmp_ge_i32 s95, s94
	s_cbranch_scc1 .Lep_go
	s_add_i32 s95, s95, 1
	s_cmp_ge_i32 s95, s94
	s_cbranch_scc1 .Lep_near
	s_sleep 6
.Lep_near:
	s_sleep 2
	s_add_i32 s73, s73, 1
	s_cmp_lt_u32 s73, 0x40000
	s_cbranch_scc1 .Lep_wait
